# batch6 with the hot MFMA loops padded back to the baseline's byte offsets (unreachable s_nop pads behind unconditional branches)
# baseline (speedup 1.0000x reference)
.LBB0_401:
	s_or_b64 exec, exec, s[38:39]
	v_mul_f32_e64 v32, v29, -v35
	ds_bpermute_b32 v33, v96, v32
	v_or_b32_e32 v125, s42, v69
	v_cmp_eq_u32_e32 vcc, 0, v125
	s_and_b32 s43, s54, 7
	s_lshl_b32 s38, s43, 9
	s_waitcnt lgkmcnt(0)
	v_fma_f32 v33, v29, -v35, v33
	v_cndmask_b32_e64 v32, v33, v32, s[0:1]
	ds_bpermute_b32 v33, v97, v32
	s_waitcnt vmcnt(26)
	v_cndmask_b32_e64 v20, v20, 0, vcc
	s_waitcnt vmcnt(25)
	v_cndmask_b32_e64 v126, v30, 0, vcc
	s_waitcnt vmcnt(24)
	v_cndmask_b32_e64 v134, v31, 0, vcc
	v_lshlrev_b32_e32 v30, 16, v20
	s_waitcnt lgkmcnt(0)
	v_add_f32_e32 v33, v32, v33
	v_cndmask_b32_e64 v32, v33, v32, s[14:15]
	ds_bpermute_b32 v33, v98, v32
	v_and_b32_e32 v31, 0xffff0000, v20
	s_waitcnt vmcnt(0)
	v_fma_f32 v128, v4, v30, v6
	v_or_b32_e32 v35, s38, v1
	v_readlane_b32 s60, v253, 18
	s_waitcnt lgkmcnt(0)
	v_add_f32_e32 v33, v32, v33
	v_cndmask_b32_e64 v32, v33, v32, s[4:5]
	ds_bpermute_b32 v33, v99, v32
	v_readlane_b32 s70, v253, 28
	v_readlane_b32 s71, v253, 29
	v_fma_f32 v135, v5, v31, v7
	v_lshlrev_b32_e32 v125, 16, v126
	s_waitcnt lgkmcnt(0)
	v_add_f32_e32 v20, v32, v33
	v_cndmask_b32_e64 v32, v20, v32, s[6:7]
	ds_bpermute_b32 v33, v100, v32
	v_lshlrev_b32_e32 v20, 2, v35
	v_lshlrev_b32_e32 v130, 16, v122
	v_lshlrev_b32_e32 v131, 16, v134
	v_fmac_f32_e32 v128, v8, v125
	s_waitcnt lgkmcnt(0)
	v_add_f32_e32 v30, v32, v33
	v_cndmask_b32_e64 v127, v30, v32, s[8:9]
	ds_bpermute_b32 v129, v101, v127
	v_lshl_add_u64 v[30:31], s[30:31], 0, v[20:21]
	v_lshl_add_u64 v[32:33], s[70:71], 0, v[20:21]
	v_lshlrev_b32_e32 v20, 1, v35
	v_and_b32_e32 v122, 0xffff0000, v122
	s_waitcnt lgkmcnt(0)
	v_add_f32_e32 v35, v127, v129
	v_cndmask_b32_e64 v35, v35, v127, s[10:11]
	v_add_f32_e32 v34, v35, v34
	ds_write2st64_b32 v84, v29, v34 offset0:1 offset1:17
	v_mov_b32_e32 v34, v36
	v_mov_b32_e32 v35, v2
	v_pk_mul_f32 v[132:133], v[34:35], v[130:131]
	v_and_b32_e32 v127, 0xffff0000, v126
	v_add_f32_e32 v2, v133, v128
	v_add_f32_e32 v29, v132, v2
	v_mul_f32_e32 v2, 0xbfb8aa3b, v29
	v_exp_f32_e32 v2, v2
	v_lshlrev_b32_e32 v129, 16, v123
	v_lshlrev_b32_e32 v128, 16, v124
	v_and_b32_e32 v133, 0xffff0000, v123
	v_add_f32_e32 v2, 1.0, v2
	v_and_b32_e32 v132, 0xffff0000, v124
	v_rcp_f32_e32 v124, v2
	v_and_b32_e32 v123, 0xffff0000, v134
	v_mov_b32_e32 v2, v37
	v_fmac_f32_e32 v135, v9, v127
	v_pk_mul_f32 v[36:37], v[2:3], v[122:123]
	v_mul_f32_e32 v29, v29, v124
	v_add_f32_e32 v37, v37, v135
	v_add_f32_e32 v126, v36, v37
	v_mul_f32_e32 v36, 0xbfb8aa3b, v126
	v_exp_f32_e32 v134, v36
	v_mov_b32_e32 v37, v4
	v_mov_b32_e32 v36, v8
	v_mov_b32_e32 v124, v131
	v_add_f32_e32 v4, 1.0, v134
	v_rcp_f32_e32 v4, v4
	v_pk_mul_f32 v[124:125], v[36:37], v[124:125]
	v_pk_mul_f32 v[134:135], v[36:37], v[130:131]
	v_add_f32_e32 v125, v125, v6
	v_mul_f32_e32 v138, v126, v4
	v_mov_b32_e32 v4, v9
	v_mov_b32_e32 v126, v123
	v_pk_mul_f32 v[8:9], v[4:5], v[126:127]
	v_pk_mov_b32 v[126:127], v[128:129], v[130:131] op_sel:[1,0]
	v_add_f32_e32 v124, v124, v125
	v_pk_mul_f32 v[130:131], v[34:35], v[126:127]
	v_add_f32_e32 v135, v135, v6
	v_add_f32_e32 v124, v131, v124
	v_add_f32_e32 v139, v130, v124
	v_mul_f32_e32 v124, 0xbfb8aa3b, v139
	v_exp_f32_e32 v136, v124
	v_add_f32_e32 v134, v134, v135
	v_lshlrev_b32_e32 v131, 16, v120
	v_and_b32_e32 v135, 0xffff0000, v120
	v_add_f32_e32 v136, 1.0, v136
	v_rcp_f32_e32 v140, v136
	v_pk_mul_f32 v[136:137], v[34:35], v[128:129]
	v_lshlrev_b32_e32 v130, 16, v121
	v_add_f32_e32 v134, v137, v134
	v_add_f32_e32 v136, v136, v134
	v_mul_f32_e32 v134, 0xbfb8aa3b, v136
	v_exp_f32_e32 v137, v134
	v_and_b32_e32 v134, 0xffff0000, v121
	v_add_f32_e32 v9, v9, v7
	v_pk_mul_f32 v[124:125], v[4:5], v[122:123]
	v_add_f32_e32 v120, 1.0, v137
	v_rcp_f32_e32 v137, v120
	v_pk_mov_b32 v[120:121], v[132:133], v[122:123] op_sel:[1,0]
	v_add_f32_e32 v8, v8, v9
	v_pk_mul_f32 v[122:123], v[2:3], v[120:121]
	v_mul_f32_e32 v139, v139, v140
	v_add_f32_e32 v8, v123, v8
	v_add_f32_e32 v140, v122, v8
	v_mul_f32_e32 v8, 0xbfb8aa3b, v140
	v_add_f32_e32 v123, v125, v7
	v_exp_f32_e32 v122, v8
	v_pk_mul_f32 v[8:9], v[2:3], v[132:133]
	v_add_f32_e32 v123, v124, v123
	v_add_f32_e32 v9, v9, v123
	v_add_f32_e32 v124, v8, v9
	v_mul_f32_e32 v8, 0xbfb8aa3b, v124
	v_exp_f32_e32 v8, v8
	v_add_f32_e32 v9, 1.0, v122
	v_mul_f32_e32 v136, v136, v137
	v_rcp_f32_e32 v125, v9
	v_add_f32_e32 v8, 1.0, v8
	v_rcp_f32_e32 v137, v8
	v_pk_mul_f32 v[8:9], v[36:37], v[126:127]
	v_mul_f32_e32 v140, v140, v125
	v_add_f32_e32 v9, v9, v6
	v_mul_f32_e32 v137, v124, v137
	v_pk_mov_b32 v[124:125], v[130:131], v[128:129] op_sel:[1,0]
	v_add_f32_e32 v8, v8, v9
	v_pk_mul_f32 v[126:127], v[34:35], v[124:125]
	v_pk_mul_f32 v[122:123], v[36:37], v[128:129]
	v_add_f32_e32 v8, v127, v8
	v_add_f32_e32 v141, v126, v8
	v_mul_f32_e32 v8, 0xbfb8aa3b, v141
	v_exp_f32_e32 v128, v8
	v_add_f32_e32 v123, v123, v6
	v_add_f32_e32 v122, v122, v123
	v_pk_mul_f32 v[120:121], v[4:5], v[120:121]
	v_add_f32_e32 v128, 1.0, v128
	v_rcp_f32_e32 v142, v128
	v_pk_mul_f32 v[128:129], v[34:35], v[130:131]
	v_lshlrev_b32_e32 v127, 16, v118
	v_add_f32_e32 v122, v129, v122
	v_add_f32_e32 v143, v128, v122
	v_mul_f32_e32 v122, 0xbfb8aa3b, v143
	v_exp_f32_e32 v128, v122
	v_and_b32_e32 v123, 0xffff0000, v118
	v_lshlrev_b32_e32 v126, 16, v119
	v_and_b32_e32 v122, 0xffff0000, v119
	v_add_f32_e32 v118, 1.0, v128
	v_mul_f32_e32 v141, v141, v142
	v_rcp_f32_e32 v142, v118
	v_pk_mov_b32 v[118:119], v[134:135], v[132:133] op_sel:[1,0]
	v_add_f32_e32 v121, v121, v7
	v_pk_mul_f32 v[128:129], v[2:3], v[118:119]
	v_add_f32_e32 v120, v120, v121
	v_add_f32_e32 v120, v129, v120
	v_pk_mul_f32 v[8:9], v[4:5], v[132:133]
	v_add_f32_e32 v132, v128, v120
	v_mul_f32_e32 v120, 0xbfb8aa3b, v132
	v_exp_f32_e32 v128, v120
	v_add_f32_e32 v9, v9, v7
	v_add_f32_e32 v8, v8, v9
	v_mul_f32_e32 v142, v143, v142
	v_add_f32_e32 v128, 1.0, v128
	v_rcp_f32_e32 v133, v128
	v_pk_mul_f32 v[128:129], v[2:3], v[134:135]
	v_pk_mul_f32 v[120:121], v[36:37], v[124:125]
	v_add_f32_e32 v8, v129, v8
	v_add_f32_e32 v143, v128, v8
	v_mul_f32_e32 v8, 0xbfb8aa3b, v143
	v_exp_f32_e32 v144, v8
	v_pk_mov_b32 v[8:9], v[126:127], v[130:131] op_sel:[1,0]
	v_add_f32_e32 v121, v121, v6
	v_pk_mul_f32 v[128:129], v[34:35], v[8:9]
	v_add_f32_e32 v120, v120, v121
	v_add_f32_e32 v120, v129, v120
	v_add_f32_e32 v128, v128, v120
	v_mul_f32_e32 v120, 0xbfb8aa3b, v128
	v_exp_f32_e32 v120, v120
	v_pk_mul_f32 v[118:119], v[4:5], v[118:119]
	v_pk_mul_f32 v[124:125], v[36:37], v[130:131]
	v_pk_mov_b32 v[130:131], v[122:123], v[134:135] op_sel:[1,0]
	v_add_f32_e32 v120, 1.0, v120
	v_rcp_f32_e32 v129, v120
	v_add_f32_e32 v119, v119, v7
	v_add_f32_e32 v121, 1.0, v144
	v_mul_f32_e32 v144, v132, v133
	v_pk_mul_f32 v[132:133], v[2:3], v[130:131]
	v_add_f32_e32 v118, v118, v119
	v_add_f32_e32 v118, v133, v118
	v_mul_f32_e32 v145, v128, v129
	v_pk_mul_f32 v[128:129], v[34:35], v[126:127]
	v_add_f32_e32 v127, v132, v118
	v_rcp_f32_e32 v121, v121
	v_mul_f32_e32 v118, 0xbfb8aa3b, v127
	v_exp_f32_e32 v118, v118
	v_add_f32_e32 v125, v125, v6
	v_mul_f32_e32 v143, v143, v121
	v_pk_mul_f32 v[120:121], v[4:5], v[134:135]
	v_add_f32_e32 v119, v124, v125
	v_add_f32_e32 v119, v129, v119
	v_add_f32_e32 v118, 1.0, v118
	v_add_f32_e32 v121, v121, v7
	v_add_f32_e32 v124, v128, v119
	v_rcp_f32_e32 v125, v118
	v_pk_mul_f32 v[118:119], v[2:3], v[122:123]
	v_add_f32_e32 v120, v120, v121
	v_add_f32_e32 v119, v119, v120
	v_add_f32_e32 v123, v118, v119
	v_mul_f32_e32 v118, 0xbfb8aa3b, v124
	v_exp_f32_e32 v118, v118
	v_mul_f32_e32 v119, 0xbfb8aa3b, v123
	v_exp_f32_e32 v119, v119
	v_pk_mul_f32 v[8:9], v[36:37], v[8:9]
	v_lshlrev_b32_e32 v120, 16, v117
	v_mov_b32_e32 v121, v126
	v_add_f32_e32 v9, v9, v6
	v_add_f32_e32 v118, 1.0, v118
	v_pk_mul_f32 v[120:121], v[34:35], v[120:121]
	v_add_f32_e32 v8, v8, v9
	v_mul_f32_e32 v125, v127, v125
	v_rcp_f32_e32 v127, v118
	v_add_f32_e32 v128, 1.0, v119
	v_pk_mul_f32 v[118:119], v[4:5], v[130:131]
	v_add_f32_e32 v8, v121, v8
	v_add_f32_e32 v120, v120, v8
	v_and_b32_e32 v8, 0xffff0000, v117
	v_mov_b32_e32 v9, v122
	v_add_f32_e32 v117, v119, v7
	v_pk_mul_f32 v[8:9], v[2:3], v[8:9]
	v_add_f32_e32 v117, v118, v117
	v_add_f32_e32 v9, v9, v117
	v_add_f32_e32 v8, v8, v9
	v_mul_f32_e32 v9, 0xbfb8aa3b, v120
	v_mul_f32_e32 v117, 0xbfb8aa3b, v8
	v_exp_f32_e32 v9, v9
	v_exp_f32_e32 v117, v117
	v_rcp_f32_e32 v118, v128
	v_mul_f32_e32 v121, v124, v127
	v_add_f32_e32 v9, 1.0, v9
	v_add_f32_e32 v117, 1.0, v117
	v_rcp_f32_e32 v9, v9
	v_rcp_f32_e32 v117, v117
	v_mul_f32_e32 v126, v123, v118
	v_cvt_pk_bf16_f32 v118, v29, v139
	v_mul_f32_e32 v9, v120, v9
	v_mul_f32_e32 v8, v8, v117
	v_cvt_pk_bf16_f32 v119, v136, v141
	v_cvt_pk_bf16_f32 v120, v142, v145
	v_cvt_pk_bf16_f32 v121, v121, v9
	v_cvt_pk_bf16_f32 v122, v138, v140
	v_cvt_pk_bf16_f32 v123, v137, v144
	v_cvt_pk_bf16_f32 v124, v143, v125
	v_cvt_pk_bf16_f32 v125, v126, v8
	v_lshlrev_b32_e32 v8, 16, v116
	v_lshlrev_b32_e32 v9, 16, v113
	ds_write_b128 v85, v[118:121] offset:8192
	ds_write_b128 v85, v[122:125] offset:8464
	v_pk_mul_f32 v[118:119], v[36:37], v[8:9]
	v_lshlrev_b32_e32 v123, 16, v114
	v_lshlrev_b32_e32 v122, 16, v57
	v_add_f32_e32 v9, v119, v6
	v_pk_mul_f32 v[126:127], v[34:35], v[122:123]
	v_add_f32_e32 v9, v118, v9
	v_add_f32_e32 v9, v127, v9
	v_and_b32_e32 v117, 0xffff0000, v113
	v_and_b32_e32 v116, 0xffff0000, v116
	v_add_f32_e32 v9, v126, v9
	v_pk_mul_f32 v[120:121], v[4:5], v[116:117]
	v_mul_f32_e32 v29, 0xbfb8aa3b, v9
	v_and_b32_e32 v125, 0xffff0000, v114
	v_exp_f32_e32 v29, v29
	v_and_b32_e32 v124, 0xffff0000, v57
	v_add_f32_e32 v57, v121, v7
	v_pk_mul_f32 v[126:127], v[2:3], v[124:125]
	v_add_f32_e32 v57, v120, v57
	v_add_f32_e32 v57, v127, v57
	v_add_f32_e32 v57, v126, v57
	v_add_f32_e32 v29, 1.0, v29
	v_mul_f32_e32 v113, 0xbfb8aa3b, v57
	v_rcp_f32_e32 v29, v29
	v_exp_f32_e32 v114, v113
	v_lshlrev_b32_e32 v119, 16, v112
	v_lshlrev_b32_e32 v118, 16, v115
	v_mul_f32_e32 v29, v9, v29
	v_add_f32_e32 v9, 1.0, v114
	v_rcp_f32_e32 v120, v9
	v_pk_mov_b32 v[8:9], v[122:123], v[8:9] op_sel:[1,0]
	v_and_b32_e32 v113, 0xffff0000, v112
	v_pk_mul_f32 v[8:9], v[36:37], v[8:9]
	v_mul_f32_e32 v128, v57, v120
	v_pk_mov_b32 v[120:121], v[118:119], v[122:123] op_sel:[1,0]
	v_add_f32_e32 v9, v9, v6
	v_and_b32_e32 v112, 0xffff0000, v115
	v_pk_mul_f32 v[114:115], v[36:37], v[122:123]
	v_pk_mul_f32 v[122:123], v[34:35], v[120:121]
	v_add_f32_e32 v8, v8, v9
	v_add_f32_e32 v8, v123, v8
	v_add_f32_e32 v129, v122, v8
	v_mul_f32_e32 v8, 0xbfb8aa3b, v129
	v_exp_f32_e32 v57, v8
	v_pk_mul_f32 v[126:127], v[34:35], v[118:119]
	v_pk_mov_b32 v[116:117], v[124:125], v[116:117] op_sel:[1,0]
	v_lshlrev_b32_e32 v123, 16, v55
	v_add_f32_e32 v57, 1.0, v57
	v_rcp_f32_e32 v130, v57
	v_add_f32_e32 v57, v115, v6
	v_add_f32_e32 v57, v114, v57
	v_add_f32_e32 v57, v127, v57
	v_add_f32_e32 v126, v126, v57
	v_mul_f32_e32 v57, 0xbfb8aa3b, v126
	v_exp_f32_e32 v114, v57
	v_pk_mul_f32 v[116:117], v[4:5], v[116:117]
	v_and_b32_e32 v57, 0xffff0000, v55
	v_add_f32_e32 v117, v117, v7
	v_add_f32_e32 v55, 1.0, v114
	v_pk_mov_b32 v[114:115], v[112:113], v[124:125] op_sel:[1,0]
	v_pk_mul_f32 v[8:9], v[4:5], v[124:125]
	v_pk_mul_f32 v[124:125], v[2:3], v[114:115]
	v_add_f32_e32 v116, v116, v117
	v_add_f32_e32 v116, v125, v116
	v_add_f32_e32 v124, v124, v116
	v_mul_f32_e32 v116, 0xbfb8aa3b, v124
	v_add_f32_e32 v9, v9, v7
	v_exp_f32_e32 v125, v116
	v_pk_mul_f32 v[116:117], v[2:3], v[112:113]
	v_add_f32_e32 v8, v8, v9
	v_add_f32_e32 v8, v117, v8
	v_mul_f32_e32 v127, v129, v130
	v_add_f32_e32 v129, v116, v8
	v_mul_f32_e32 v8, 0xbfb8aa3b, v129
	v_exp_f32_e32 v8, v8
	v_rcp_f32_e32 v55, v55
	v_add_f32_e32 v9, 1.0, v125
	v_lshlrev_b32_e32 v122, 16, v56
	v_add_f32_e32 v8, 1.0, v8
	v_mul_f32_e32 v126, v126, v55
	v_rcp_f32_e32 v55, v9
	v_rcp_f32_e32 v125, v8
	v_pk_mul_f32 v[8:9], v[36:37], v[120:121]
	v_pk_mul_f32 v[116:117], v[36:37], v[118:119]
	v_pk_mov_b32 v[118:119], v[122:123], v[118:119] op_sel:[1,0]
	v_add_f32_e32 v9, v9, v6
	v_pk_mul_f32 v[120:121], v[34:35], v[118:119]
	v_add_f32_e32 v8, v8, v9
	v_add_f32_e32 v8, v121, v8
	v_add_f32_e32 v131, v120, v8
	v_mul_f32_e32 v8, 0xbfb8aa3b, v131
	v_mul_f32_e32 v130, v124, v55
	v_exp_f32_e32 v55, v8
	v_mul_f32_e32 v129, v129, v125
	v_pk_mul_f32 v[124:125], v[34:35], v[122:123]
	v_and_b32_e32 v56, 0xffff0000, v56
	v_add_f32_e32 v55, 1.0, v55
	v_rcp_f32_e32 v132, v55
	v_add_f32_e32 v55, v117, v6
	v_add_f32_e32 v55, v116, v55
	v_add_f32_e32 v55, v125, v55
	v_add_f32_e32 v124, v124, v55
	v_mul_f32_e32 v55, 0xbfb8aa3b, v124
	v_exp_f32_e32 v116, v55
	v_pk_mul_f32 v[114:115], v[4:5], v[114:115]
	v_pk_mul_f32 v[8:9], v[4:5], v[112:113]
	v_pk_mov_b32 v[112:113], v[56:57], v[112:113] op_sel:[1,0]
	v_add_f32_e32 v116, 1.0, v116
	v_add_f32_e32 v115, v115, v7
	v_rcp_f32_e32 v125, v116
	v_pk_mul_f32 v[116:117], v[2:3], v[112:113]
	v_add_f32_e32 v114, v114, v115
	v_add_f32_e32 v114, v117, v114
	v_lshlrev_b32_e32 v121, 16, v53
	v_and_b32_e32 v55, 0xffff0000, v53
	v_mul_f32_e32 v53, v131, v132
	v_add_f32_e32 v131, v116, v114
	v_mul_f32_e32 v114, 0xbfb8aa3b, v131
	v_exp_f32_e32 v132, v114
	v_pk_mul_f32 v[114:115], v[36:37], v[118:119]
	v_add_f32_e32 v9, v9, v7
	v_mul_f32_e32 v124, v124, v125
	v_add_f32_e32 v118, 1.0, v132
	v_rcp_f32_e32 v125, v118
	v_pk_mul_f32 v[118:119], v[2:3], v[56:57]
	v_add_f32_e32 v8, v8, v9
	v_add_f32_e32 v8, v119, v8
	v_add_f32_e32 v132, v118, v8
	v_lshlrev_b32_e32 v120, 16, v54
	v_mul_f32_e32 v8, 0xbfb8aa3b, v132
	v_exp_f32_e32 v133, v8
	v_pk_mov_b32 v[8:9], v[120:121], v[122:123] op_sel:[1,0]
	v_add_f32_e32 v115, v115, v6
	v_pk_mul_f32 v[118:119], v[34:35], v[8:9]
	v_add_f32_e32 v114, v114, v115
	v_add_f32_e32 v114, v119, v114
	v_add_f32_e32 v118, v118, v114
	v_mul_f32_e32 v114, 0xbfb8aa3b, v118
	v_exp_f32_e32 v114, v114
	v_add_f32_e32 v115, 1.0, v133
	v_rcp_f32_e32 v115, v115
	v_and_b32_e32 v54, 0xffff0000, v54
	v_add_f32_e32 v114, 1.0, v114
	v_rcp_f32_e32 v119, v114
	v_pk_mul_f32 v[112:113], v[4:5], v[112:113]
	v_mul_f32_e32 v125, v131, v125
	v_mul_f32_e32 v131, v132, v115
	v_pk_mul_f32 v[114:115], v[4:5], v[56:57]
	v_pk_mov_b32 v[56:57], v[54:55], v[56:57] op_sel:[1,0]
	v_add_f32_e32 v113, v113, v7
	v_pk_mul_f32 v[116:117], v[36:37], v[122:123]
	v_pk_mul_f32 v[122:123], v[2:3], v[56:57]
	v_add_f32_e32 v112, v112, v113
	v_add_f32_e32 v112, v123, v112
	v_mul_f32_e32 v132, v118, v119
	v_pk_mul_f32 v[118:119], v[34:35], v[120:121]
	v_add_f32_e32 v121, v122, v112
	v_mul_f32_e32 v112, 0xbfb8aa3b, v121
	v_exp_f32_e32 v112, v112
	v_add_f32_e32 v117, v117, v6
	v_add_f32_e32 v113, v116, v117
	v_add_f32_e32 v113, v119, v113
	v_add_f32_e32 v112, 1.0, v112
	v_pk_mul_f32 v[8:9], v[36:37], v[8:9]
	v_add_f32_e32 v116, v118, v113
	v_rcp_f32_e32 v117, v112
	v_pk_mul_f32 v[112:113], v[2:3], v[54:55]
	v_add_f32_e32 v55, v115, v7
	v_pk_mul_f32 v[4:5], v[4:5], v[56:57]
	v_lshlrev_b32_e32 v36, 16, v52
	v_mov_b32_e32 v37, v120
	v_add_f32_e32 v6, v9, v6
	v_add_f32_e32 v55, v114, v55
	v_pk_mul_f32 v[34:35], v[34:35], v[36:37]
	v_add_f32_e32 v6, v8, v6
	v_and_b32_e32 v8, 0xffff0000, v52
	v_mov_b32_e32 v9, v54
	v_add_f32_e32 v5, v5, v7
	v_add_f32_e32 v55, v113, v55
	v_add_f32_e32 v6, v35, v6
	v_pk_mul_f32 v[2:3], v[2:3], v[8:9]
	v_add_f32_e32 v4, v4, v5
	v_add_f32_e32 v55, v112, v55
	v_add_f32_e32 v6, v34, v6
	v_add_f32_e32 v3, v3, v4
	v_mul_f32_e32 v112, 0xbfb8aa3b, v116
	v_mul_f32_e32 v113, 0xbfb8aa3b, v55
	v_add_f32_e32 v2, v2, v3
	v_mul_f32_e32 v3, 0xbfb8aa3b, v6
	v_exp_f32_e32 v112, v112
	v_exp_f32_e32 v113, v113
	v_exp_f32_e32 v3, v3
	v_mul_f32_e32 v4, 0xbfb8aa3b, v2
	v_exp_f32_e32 v4, v4
	v_add_f32_e32 v112, 1.0, v112
	v_add_f32_e32 v113, 1.0, v113
	v_add_f32_e32 v3, 1.0, v3
	v_rcp_f32_e32 v112, v112
	v_rcp_f32_e32 v5, v113
	v_rcp_f32_e32 v3, v3
	v_add_f32_e32 v4, 1.0, v4
	v_rcp_f32_e32 v4, v4
	v_mul_f32_e32 v7, v116, v112
	v_mul_f32_e32 v9, v55, v5
	v_mul_f32_e32 v5, v6, v3
	v_mul_f32_e32 v114, v121, v117
	v_mul_f32_e32 v34, v2, v4
	v_cvt_pk_bf16_f32 v2, v29, v127
	v_cvt_pk_bf16_f32 v3, v126, v53
	v_cvt_pk_bf16_f32 v4, v124, v132
	v_cvt_pk_bf16_f32 v5, v7, v5
	v_cvt_pk_bf16_f32 v6, v128, v130
	v_cvt_pk_bf16_f32 v7, v129, v125
	v_cvt_pk_bf16_f32 v8, v131, v114
	v_cvt_pk_bf16_f32 v9, v9, v34
	ds_write_b128 v85, v[2:5] offset:8320
	ds_write_b128 v85, v[6:9] offset:8592
	s_waitcnt lgkmcnt(0)
	s_barrier
	v_cndmask_b32_e64 v3, v50, 0, s[12:13]
	v_cndmask_b32_e64 v9, v51, 0, s[12:13]
	ds_read_b32 v29, v21 offset:4604
	ds_read_b128 v[50:53], v86 offset:4096
	v_cndmask_b32_e64 v2, v49, 0, s[12:13]
	v_lshlrev_b32_e32 v4, 16, v2
	v_fma_f32 v36, v12, v4, v14
	v_lshlrev_b32_e32 v37, 16, v3
	s_waitcnt lgkmcnt(0)
	v_sub_f32_e32 v34, v29, v50
	v_mul_f32_e32 v34, 0x3fb8aa3b, v34
	v_exp_f32_e32 v113, v34
	v_lshlrev_b32_e32 v117, 16, v9
	v_lshlrev_b32_e32 v116, 16, v45
	v_mov_b32_e32 v34, v18
	v_mov_b32_e32 v35, v10
	v_fmac_f32_e32 v36, v16, v37
	v_pk_mul_f32 v[118:119], v[34:35], v[116:117]
	v_and_b32_e32 v2, 0xffff0000, v2
	v_add_f32_e32 v10, v119, v36
	v_add_f32_e32 v10, v118, v10
	v_mul_f32_e32 v18, 0xbfb8aa3b, v10
	v_exp_f32_e32 v18, v18
	v_fma_f32 v57, v13, v2, v15
	v_and_b32_e32 v49, 0xffff0000, v3
	v_lshlrev_b32_e32 v115, 16, v46
	v_add_f32_e32 v18, 1.0, v18
	v_rcp_f32_e32 v18, v18
	v_and_b32_e32 v119, 0xffff0000, v46
	v_and_b32_e32 v121, 0xffff0000, v9
	v_and_b32_e32 v120, 0xffff0000, v45
	v_mul_f32_e32 v46, v10, v18
	v_mov_b32_e32 v10, v19
	v_fmac_f32_e32 v57, v17, v49
	v_pk_mul_f32 v[18:19], v[10:11], v[120:121]
	ds_read_b128 v[2:5], v86
	ds_read_b96 v[6:8], v86 offset:16
	ds_read_b96 v[54:56], v86 offset:4112
	v_add_f32_e32 v9, v19, v57
	v_add_f32_e32 v18, v18, v9
	v_mul_f32_e32 v9, 0xbfb8aa3b, v18
	v_exp_f32_e32 v9, v9
	v_sub_f32_e32 v36, v29, v51
	v_lshlrev_b32_e32 v114, 16, v48
	v_and_b32_e32 v118, 0xffff0000, v48
	v_add_f32_e32 v9, 1.0, v9
	v_rcp_f32_e32 v112, v9
	v_mul_f32_e32 v36, 0x3fb8aa3b, v36
	v_mov_b32_e32 v123, v12
	s_waitcnt lgkmcnt(2)
	v_mov_b32_e32 v19, v2
	v_mov_b32_e32 v12, v17
	v_mov_b32_e32 v48, v121
	v_fma_f32 v2, v13, v49, v15
	v_exp_f32_e32 v51, v36
	v_mov_b32_e32 v122, v16
	v_mov_b32_e32 v36, v117
	v_pk_mul_f32 v[18:19], v[18:19], v[112:113]
	v_pk_fma_f32 v[16:17], v[12:13], v[48:49], v[2:3] op_sel_hi:[1,1,0]
	v_fma_f32 v2, v13, v121, v15
	v_pk_mul_f32 v[36:37], v[122:123], v[36:37]
	v_mul_f32_e32 v57, v46, v19
	v_mul_f32_e32 v126, v18, v19
	v_pk_fma_f32 v[18:19], v[12:13], v[120:121], v[2:3] op_sel_hi:[1,1,0]
	v_sub_f32_e32 v2, v29, v52
	v_mul_f32_e32 v2, 0x3fb8aa3b, v2
	v_lshlrev_b32_e32 v48, 16, v47
	v_and_b32_e32 v112, 0xffff0000, v47
	v_pk_mov_b32 v[46:47], v[114:115], v[116:117] op_sel:[1,0]
	v_add_f32_e32 v9, v37, v14
	v_exp_f32_e32 v45, v2
	v_sub_f32_e32 v2, v29, v53
	v_pk_mul_f32 v[52:53], v[34:35], v[46:47]
	v_add_f32_e32 v9, v36, v9
	v_add_f32_e32 v9, v53, v9
	v_pk_mul_f32 v[124:125], v[122:123], v[116:117]
	v_add_f32_e32 v9, v52, v9
	v_mul_f32_e32 v36, 0xbfb8aa3b, v9
	v_add_f32_e32 v50, v125, v14
	v_lshlrev_b32_e32 v49, 16, v44
	v_and_b32_e32 v113, 0xffff0000, v44
	v_exp_f32_e32 v44, v36
	v_pk_mul_f32 v[36:37], v[34:35], v[114:115]
	v_add_f32_e32 v50, v124, v50
	v_add_f32_e32 v37, v37, v50
	v_add_f32_e32 v36, v36, v37
	v_mul_f32_e32 v37, 0xbfb8aa3b, v36
	v_exp_f32_e32 v50, v37
	v_mul_f32_e32 v2, 0x3fb8aa3b, v2
	v_exp_f32_e32 v37, v2
	v_add_f32_e32 v2, 1.0, v44
	v_rcp_f32_e32 v44, v2
	v_add_f32_e32 v2, 1.0, v50
	v_pk_mov_b32 v[52:53], v[118:119], v[120:121] op_sel:[1,0]
	v_rcp_f32_e32 v50, v2
	v_mul_f32_e32 v2, v11, v53
	v_pk_add_f32 v[16:17], v[2:3], v[16:17] op_sel_hi:[0,1]
	v_pk_fma_f32 v[16:17], v[10:11], v[52:53], v[16:17]
	v_mul_f32_e32 v36, v36, v50
	v_mul_f32_e32 v2, 0xbfb8aa3b, v16
	v_exp_f32_e32 v2, v2
	v_mov_b32_e32 v17, v3
	v_mul_f32_e32 v9, v9, v44
	v_pk_mul_f32 v[46:47], v[122:123], v[46:47]
	v_add_f32_e32 v2, 1.0, v2
	v_rcp_f32_e32 v50, v2
	v_mul_f32_e32 v2, v11, v119
	v_pk_add_f32 v[18:19], v[2:3], v[18:19] op_sel_hi:[0,1]
	v_pk_fma_f32 v[18:19], v[10:11], v[118:119], v[18:19]
	v_pk_mul_f32 v[116:117], v[122:123], v[114:115]
	v_mul_f32_e32 v2, 0xbfb8aa3b, v18
	v_exp_f32_e32 v19, v2
	v_pk_mul_f32 v[2:3], v[16:17], v[50:51]
	v_and_b32_e32 v51, 0xffff0000, v41
	v_mul_f32_e32 v120, v9, v3
	v_add_f32_e32 v16, 1.0, v19
	v_rcp_f32_e32 v44, v16
	v_mov_b32_e32 v19, v4
	v_mul_f32_e32 v121, v2, v3
	v_fma_f32 v4, v13, v119, v15
	v_pk_mul_f32 v[2:3], v[18:19], v[44:45]
	v_pk_fma_f32 v[16:17], v[12:13], v[118:119], v[4:5] op_sel_hi:[1,1,0]
	v_mul_f32_e32 v125, v2, v3
	v_fma_f32 v2, v13, v53, v15
	s_waitcnt lgkmcnt(0)
	v_sub_f32_e32 v4, v29, v54
	v_mul_f32_e32 v124, v36, v3
	v_pk_fma_f32 v[2:3], v[12:13], v[52:53], v[2:3] op_sel_hi:[1,1,0]
	v_mul_f32_e32 v4, 0x3fb8aa3b, v4
	v_pk_mov_b32 v[52:53], v[48:49], v[114:115] op_sel:[1,0]
	v_add_f32_e32 v9, v47, v14
	v_exp_f32_e32 v19, v4
	v_sub_f32_e32 v4, v29, v55
	v_pk_mul_f32 v[54:55], v[34:35], v[52:53]
	v_add_f32_e32 v9, v46, v9
	v_add_f32_e32 v36, v117, v14
	v_add_f32_e32 v9, v55, v9
	v_pk_mul_f32 v[46:47], v[34:35], v[48:49]
	v_add_f32_e32 v36, v116, v36
	v_add_f32_e32 v9, v54, v9
	v_add_f32_e32 v36, v47, v36
	v_mul_f32_e32 v18, 0xbfb8aa3b, v9
	v_add_f32_e32 v36, v46, v36
	v_lshlrev_b32_e32 v45, 16, v41
	v_exp_f32_e32 v18, v18
	v_mul_f32_e32 v41, 0xbfb8aa3b, v36
	v_exp_f32_e32 v41, v41
	v_mul_f32_e32 v4, 0x3fb8aa3b, v4
	v_exp_f32_e32 v47, v4
	v_add_f32_e32 v4, 1.0, v18
	v_rcp_f32_e32 v18, v4
	v_add_f32_e32 v4, 1.0, v41
	v_pk_mov_b32 v[54:55], v[112:113], v[118:119] op_sel:[1,0]
	v_rcp_f32_e32 v41, v4
	v_mul_f32_e32 v4, v11, v55
	v_pk_add_f32 v[2:3], v[4:5], v[2:3] op_sel_hi:[0,1]
	v_pk_fma_f32 v[2:3], v[10:11], v[54:55], v[2:3]
	v_mul_f32_e32 v4, v11, v113
	v_mul_f32_e32 v3, 0xbfb8aa3b, v2
	v_exp_f32_e32 v3, v3
	v_pk_add_f32 v[16:17], v[4:5], v[16:17] op_sel_hi:[0,1]
	v_pk_fma_f32 v[16:17], v[10:11], v[112:113], v[16:17]
	v_mul_f32_e32 v41, v36, v41
	v_add_f32_e32 v3, 1.0, v3
	v_rcp_f32_e32 v36, v3
	v_mul_f32_e32 v3, 0xbfb8aa3b, v16
	v_exp_f32_e32 v4, v3
	v_mul_f32_e32 v9, v9, v18
	v_lshlrev_b32_e32 v44, 16, v43
	v_pk_mul_f32 v[52:53], v[122:123], v[52:53]
	v_add_f32_e32 v4, 1.0, v4
	v_rcp_f32_e32 v18, v4
	v_mov_b32_e32 v3, v5
	v_pk_mul_f32 v[2:3], v[2:3], v[36:37]
	v_mov_b32_e32 v17, v6
	v_pk_mov_b32 v[4:5], v[44:45], v[48:49] op_sel:[1,0]
	v_add_f32_e32 v6, v53, v14
	v_and_b32_e32 v50, 0xffff0000, v43
	v_mul_f32_e32 v43, v9, v3
	v_mul_f32_e32 v116, v2, v3
	v_pk_mul_f32 v[2:3], v[16:17], v[18:19]
	v_pk_mul_f32 v[16:17], v[34:35], v[4:5]
	v_add_f32_e32 v6, v52, v6
	v_add_f32_e32 v6, v17, v6
	v_add_f32_e32 v9, v16, v6
	v_mul_f32_e32 v6, 0xbfb8aa3b, v9
	v_exp_f32_e32 v6, v6
	v_pk_mul_f32 v[114:115], v[122:123], v[48:49]
	v_mul_f32_e32 v41, v41, v3
	v_mul_f32_e32 v48, v2, v3
	v_add_f32_e32 v3, 1.0, v6
	v_rcp_f32_e32 v18, v3
	v_fma_f32 v2, v13, v55, v15
	v_fma_f32 v6, v13, v113, v15
	v_pk_fma_f32 v[2:3], v[12:13], v[54:55], v[2:3] op_sel_hi:[1,1,0]
	v_mul_f32_e32 v9, v9, v18
	v_pk_mov_b32 v[18:19], v[50:51], v[112:113] op_sel:[1,0]
	v_pk_fma_f32 v[16:17], v[12:13], v[112:113], v[6:7] op_sel_hi:[1,1,0]
	v_mul_f32_e32 v6, v11, v19
	v_pk_add_f32 v[2:3], v[6:7], v[2:3] op_sel_hi:[0,1]
	v_pk_fma_f32 v[2:3], v[10:11], v[18:19], v[2:3]
	v_add_f32_e32 v6, v115, v14
	v_mul_f32_e32 v3, 0xbfb8aa3b, v2
	v_exp_f32_e32 v3, v3
	v_pk_mul_f32 v[36:37], v[34:35], v[44:45]
	v_add_f32_e32 v6, v114, v6
	v_pk_mul_f32 v[4:5], v[122:123], v[4:5]
	v_add_f32_e32 v3, 1.0, v3
	v_rcp_f32_e32 v46, v3
	v_add_f32_e32 v3, v37, v6
	v_add_f32_e32 v36, v36, v3
	v_mov_b32_e32 v3, v7
	v_mul_f32_e32 v6, v11, v51
	v_pk_mul_f32 v[2:3], v[2:3], v[46:47]
	v_pk_add_f32 v[6:7], v[6:7], v[16:17] op_sel_hi:[0,1]
	v_mul_f32_e32 v37, v9, v3
	v_pk_fma_f32 v[6:7], v[10:11], v[50:51], v[6:7]
	v_mul_f32_e32 v9, 0xbfb8aa3b, v36
	v_exp_f32_e32 v9, v9
	v_mul_f32_e32 v16, 0xbfb8aa3b, v6
	v_exp_f32_e32 v16, v16
	v_sub_f32_e32 v7, v29, v56
	v_mul_f32_e32 v7, 0x3fb8aa3b, v7
	v_exp_f32_e32 v17, v7
	v_add_f32_e32 v7, 1.0, v9
	v_rcp_f32_e32 v7, v7
	v_add_f32_e32 v9, 1.0, v16
	v_rcp_f32_e32 v16, v9
	v_mul_f32_e32 v45, v2, v3
	v_mul_f32_e32 v9, v36, v7
	v_mov_b32_e32 v7, v8
	v_pk_mul_f32 v[2:3], v[6:7], v[16:17]
	v_lshlrev_b32_e32 v8, 16, v39
	v_mul_f32_e32 v16, v9, v3
	v_mov_b32_e32 v9, v44
	v_add_f32_e32 v5, v5, v14
	v_pk_mul_f32 v[8:9], v[34:35], v[8:9]
	v_add_f32_e32 v4, v4, v5
	v_fma_f32 v6, v13, v19, v15
	v_add_f32_e32 v4, v9, v4
	v_pk_fma_f32 v[6:7], v[12:13], v[18:19], v[6:7] op_sel_hi:[1,1,0]
	v_add_f32_e32 v13, v8, v4
	ds_read2st64_b32 v[8:9], v88 offset1:16
	v_mul_f32_e32 v12, v11, v50
	v_and_b32_e32 v4, 0xffff0000, v39
	v_mov_b32_e32 v5, v50
	v_pk_add_f32 v[6:7], v[12:13], v[6:7] op_sel_hi:[0,1]
	v_pk_fma_f32 v[4:5], v[10:11], v[4:5], v[6:7]
	v_mul_f32_e32 v6, 0xbfb8aa3b, v13
	v_exp_f32_e32 v6, v6
	v_mul_f32_e32 v7, 0xbfb8aa3b, v4
	s_waitcnt lgkmcnt(0)
	v_sub_f32_e32 v5, v29, v9
	v_exp_f32_e32 v9, v7
	v_mul_f32_e32 v5, 0x3fb8aa3b, v5
	s_lshr_b32 s39, s55, 3
	v_exp_f32_e32 v7, v5
	v_add_f32_e32 v5, 1.0, v6
	s_and_b32 s39, s39, 63
	v_rcp_f32_e32 v5, v5
	v_add_f32_e32 v6, 1.0, v9
	s_lshl_b32 s58, s39, 7
	v_rcp_f32_e32 v6, v6
	s_add_i32 s58, s58, s41
	v_add_u32_e32 v18, s58, v67
	v_mul_f32_e32 v10, v13, v5
	v_mov_b32_e32 v5, v8
	s_lshl_b32 s60, s40, 6
	s_lshl_b32 s59, s40, 12
	v_mad_i64_i32 v[18:19], s[40:41], v18, s45, v[20:21]
	v_mul_f32_e32 v9, v2, v3
	v_pk_mul_f32 v[2:3], v[4:5], v[6:7]
	v_lshl_add_u64 v[34:35], v[18:19], 0, s[34:35]
	v_add_u32_e32 v18, s58, v23
	v_mul_f32_e32 v5, v10, v3
	v_mul_f32_e32 v10, v2, v3
	v_cvt_pk_bf16_f32 v2, v57, v120
	v_cvt_pk_bf16_f32 v3, v124, v43
	v_cvt_pk_bf16_f32 v4, v41, v37
	v_mad_i64_i32 v[36:37], s[40:41], v18, s45, v[20:21]
	v_add_u32_e32 v18, s58, v38
	v_mad_i64_i32 v[18:19], s[40:41], v18, s45, v[20:21]
	v_lshl_add_u64 v[38:39], v[18:19], 0, s[34:35]
	v_add_u32_e32 v18, s58, v40
	v_mad_i64_i32 v[18:19], s[40:41], v18, s45, v[20:21]
	v_lshl_add_u64 v[40:41], v[18:19], 0, s[34:35]
	v_add_u32_e32 v18, s58, v42
	s_lshl_b32 s42, s43, 3
	s_lshl_b32 s43, s39, 6
	v_mad_i64_i32 v[18:19], s[40:41], v18, s45, v[20:21]
	s_or_b32 s40, s59, s43
	s_or_b32 s40, s40, s42
	s_ashr_i32 s41, s40, 31
	v_cvt_pk_bf16_f32 v5, v16, v5
	s_lshl_b64 s[40:41], s[40:41], 2
	v_readlane_b32 s61, v253, 19
	v_cvt_pk_bf16_f32 v6, v126, v121
	v_cvt_pk_bf16_f32 v7, v125, v116
	v_cvt_pk_bf16_f32 v8, v48, v45
	v_cvt_pk_bf16_f32 v9, v9, v10
	ds_write_b128 v91, v[2:5] offset:43008
	ds_write_b128 v91, v[6:9] offset:43280
	s_add_u32 s58, s40, 0x66000000
	ds_read_b128 v[14:17], v106 offset:8192
	ds_read_b128 v[10:13], v106 offset:8256
	ds_read_b128 v[6:9], v106 offset:8320
	ds_read_b128 v[2:5], v106 offset:8384
	s_addc_u32 s61, s41, 0
	s_or_b32 s40, s60, s39
	s_ashr_i32 s41, s40, 31
	s_lshl_b64 s[40:41], s[40:41], 12
	v_lshl_add_u64 v[42:43], v[18:19], 0, s[34:35]
	v_or_b32_e32 v18, s40, v22
	v_mov_b32_e32 v19, s41
	v_or_b32_e32 v18, s38, v18
	v_readlane_b32 s62, v253, 20
	v_lshlrev_b64 v[18:19], 8, v[18:19]
	s_mov_b32 s26, 0
	v_lshl_add_u64 v[44:45], v[26:27], 0, v[18:19]
	s_mov_b64 s[38:39], 0
	s_mov_b32 s62, 0
	v_readlane_b32 s63, v253, 21
	v_readlane_b32 s64, v253, 22
	v_readlane_b32 s65, v253, 23
	v_readlane_b32 s66, v253, 24
	v_readlane_b32 s67, v253, 25
	v_readlane_b32 s68, v253, 26
	v_readlane_b32 s69, v253, 27
	v_readlane_b32 s72, v253, 30
	v_readlane_b32 s73, v253, 31
	v_readlane_b32 s74, v253, 32
	v_readlane_b32 s75, v253, 33
	s_waitcnt lgkmcnt(0)
	s_barrier
	s_branch .LBB0_403
	s_nop 0
	s_nop 0
	s_nop 0
	s_nop 0
	s_nop 0
	s_nop 0
	s_nop 0
	s_nop 0
	s_nop 0
	s_nop 0
	s_nop 0
	s_nop 0
	s_nop 0
	s_nop 0
	s_nop 0
	s_nop 0
	s_nop 0
	s_nop 0
	s_nop 0
	s_nop 0
	s_nop 0
	s_nop 0
	s_nop 0
	s_nop 0
	s_nop 0
	s_nop 0
	s_nop 0
	s_nop 0
	s_nop 0
	s_nop 0
	s_nop 0
	s_nop 0
	s_nop 0
	s_nop 0
	s_nop 0
	s_nop 0
	s_nop 0
	s_nop 0
	s_nop 0
	s_nop 0
	s_nop 0
	s_nop 0
	s_nop 0
	s_nop 0
	s_nop 0
	s_nop 0
	s_nop 0
	s_nop 0
	s_nop 0
	s_nop 0
	s_nop 0
	s_nop 0
	s_nop 0
	s_nop 0
	s_nop 0
	s_nop 0
	s_nop 0
	s_nop 0
	s_nop 0
	s_nop 0
	s_nop 0
	s_nop 0
	s_nop 0
	s_nop 0
	s_nop 0
	s_nop 0
	s_nop 0
	s_nop 0
	s_nop 0
	s_nop 0
	s_nop 0
	s_nop 0
	s_nop 0
	s_nop 0
	s_nop 0
	s_nop 0
	s_nop 0
	s_nop 0
	s_nop 0
	s_nop 0
	s_nop 0
	s_nop 0
	s_nop 0
	s_nop 0
	s_nop 0
	s_nop 0
	s_nop 0
	s_nop 0
	s_nop 0

.LBB0_598:
	v_cndmask_b32_e64 v2, v2, 0, s[80:81]
	v_cndmask_b32_e64 v1, v1, 0, s[80:81]
	v_cndmask_b32_e64 v12, v12, 0, s[80:81]
	ds_read_b128 v[96:99], v142
	ds_read_b128 v[70:73], v142 offset:16
	v_lshlrev_b32_e32 v100, 16, v2
	v_and_b32_e32 v128, 0xffff0000, v2
	v_lshlrev_b32_e32 v101, 16, v1
	v_and_b32_e32 v129, 0xffff0000, v1
	v_lshlrev_b32_e32 v102, 16, v12
	v_and_b32_e32 v130, 0xffff0000, v12
	v_lshlrev_b32_e32 v103, 16, v3
	v_and_b32_e32 v131, 0xffff0000, v3
	v_lshlrev_b32_e32 v104, 16, v4
	v_and_b32_e32 v132, 0xffff0000, v4
	v_lshlrev_b32_e32 v105, 16, v5
	v_and_b32_e32 v133, 0xffff0000, v5
	v_lshlrev_b32_e32 v106, 16, v6
	v_and_b32_e32 v134, 0xffff0000, v6
	v_lshlrev_b32_e32 v107, 16, v7
	v_and_b32_e32 v135, 0xffff0000, v7
	v_lshlrev_b32_e32 v108, 16, v8
	v_and_b32_e32 v136, 0xffff0000, v8
	v_lshlrev_b32_e32 v109, 16, v9
	v_and_b32_e32 v137, 0xffff0000, v9
	v_lshlrev_b32_e32 v95, 16, v10
	v_and_b32_e32 v138, 0xffff0000, v10
	v_fma_f32 v148, v176, v100, v184
	v_fma_f32 v149, v177, v128, v185
	v_fmac_f32_e32 v148, v178, v101
	v_fmac_f32_e32 v149, v179, v129
	v_fmac_f32_e32 v148, v180, v102
	v_fmac_f32_e32 v149, v181, v130
	v_fmac_f32_e32 v148, v182, v103
	v_fmac_f32_e32 v149, v183, v131
	v_mul_f32_e32 v150, 0xbfb8aa3b, v148
	v_mul_f32_e32 v151, 0xbfb8aa3b, v149
	v_exp_f32_e32 v150, v150
	v_exp_f32_e32 v151, v151
	v_add_f32_e32 v150, 1.0, v150
	v_add_f32_e32 v151, 1.0, v151
	v_rcp_f32_e32 v150, v150
	v_rcp_f32_e32 v151, v151
	s_waitcnt lgkmcnt(0)
	v_mul_f32_e32 v148, v148, v150
	v_mul_f32_e32 v149, v149, v151
	v_mul_f32_e32 v100, v148, v96
	v_mul_f32_e32 v128, v149, v96
	v_fma_f32 v148, v176, v101, v184
	v_fma_f32 v149, v177, v129, v185
	v_fmac_f32_e32 v148, v178, v102
	v_fmac_f32_e32 v149, v179, v130
	v_fmac_f32_e32 v148, v180, v103
	v_fmac_f32_e32 v149, v181, v131
	v_fmac_f32_e32 v148, v182, v104
	v_fmac_f32_e32 v149, v183, v132
	v_mul_f32_e32 v150, 0xbfb8aa3b, v148
	v_mul_f32_e32 v151, 0xbfb8aa3b, v149
	v_exp_f32_e32 v150, v150
	v_exp_f32_e32 v151, v151
	v_add_f32_e32 v150, 1.0, v150
	v_add_f32_e32 v151, 1.0, v151
	v_rcp_f32_e32 v150, v150
	v_rcp_f32_e32 v151, v151
	v_mul_f32_e32 v148, v148, v150
	v_mul_f32_e32 v149, v149, v151
	v_mul_f32_e32 v101, v148, v97
	v_mul_f32_e32 v129, v149, v97
	v_fma_f32 v148, v176, v102, v184
	v_fma_f32 v149, v177, v130, v185
	v_fmac_f32_e32 v148, v178, v103
	v_fmac_f32_e32 v149, v179, v131
	v_fmac_f32_e32 v148, v180, v104
	v_fmac_f32_e32 v149, v181, v132
	v_fmac_f32_e32 v148, v182, v105
	v_fmac_f32_e32 v149, v183, v133
	v_mul_f32_e32 v150, 0xbfb8aa3b, v148
	v_mul_f32_e32 v151, 0xbfb8aa3b, v149
	v_exp_f32_e32 v150, v150
	v_exp_f32_e32 v151, v151
	v_add_f32_e32 v150, 1.0, v150
	v_add_f32_e32 v151, 1.0, v151
	v_rcp_f32_e32 v150, v150
	v_rcp_f32_e32 v151, v151
	v_mul_f32_e32 v148, v148, v150
	v_mul_f32_e32 v149, v149, v151
	v_mul_f32_e32 v102, v148, v98
	v_mul_f32_e32 v130, v149, v98
	v_fma_f32 v148, v176, v103, v184
	v_fma_f32 v149, v177, v131, v185
	v_fmac_f32_e32 v148, v178, v104
	v_fmac_f32_e32 v149, v179, v132
	v_fmac_f32_e32 v148, v180, v105
	v_fmac_f32_e32 v149, v181, v133
	v_fmac_f32_e32 v148, v182, v106
	v_fmac_f32_e32 v149, v183, v134
	v_mul_f32_e32 v150, 0xbfb8aa3b, v148
	v_mul_f32_e32 v151, 0xbfb8aa3b, v149
	v_exp_f32_e32 v150, v150
	v_exp_f32_e32 v151, v151
	v_add_f32_e32 v150, 1.0, v150
	v_add_f32_e32 v151, 1.0, v151
	v_rcp_f32_e32 v150, v150
	v_rcp_f32_e32 v151, v151
	v_mul_f32_e32 v148, v148, v150
	v_mul_f32_e32 v149, v149, v151
	v_mul_f32_e32 v103, v148, v99
	v_mul_f32_e32 v131, v149, v99
	v_fma_f32 v148, v176, v104, v184
	v_fma_f32 v149, v177, v132, v185
	v_fmac_f32_e32 v148, v178, v105
	v_fmac_f32_e32 v149, v179, v133
	v_fmac_f32_e32 v148, v180, v106
	v_fmac_f32_e32 v149, v181, v134
	v_fmac_f32_e32 v148, v182, v107
	v_fmac_f32_e32 v149, v183, v135
	v_mul_f32_e32 v150, 0xbfb8aa3b, v148
	v_mul_f32_e32 v151, 0xbfb8aa3b, v149
	v_exp_f32_e32 v150, v150
	v_exp_f32_e32 v151, v151
	v_add_f32_e32 v150, 1.0, v150
	v_add_f32_e32 v151, 1.0, v151
	v_rcp_f32_e32 v150, v150
	v_rcp_f32_e32 v151, v151
	v_mul_f32_e32 v148, v148, v150
	v_mul_f32_e32 v149, v149, v151
	v_mul_f32_e32 v104, v148, v70
	v_mul_f32_e32 v132, v149, v70
	v_fma_f32 v148, v176, v105, v184
	v_fma_f32 v149, v177, v133, v185
	v_fmac_f32_e32 v148, v178, v106
	v_fmac_f32_e32 v149, v179, v134
	v_fmac_f32_e32 v148, v180, v107
	v_fmac_f32_e32 v149, v181, v135
	v_fmac_f32_e32 v148, v182, v108
	v_fmac_f32_e32 v149, v183, v136
	v_mul_f32_e32 v150, 0xbfb8aa3b, v148
	v_mul_f32_e32 v151, 0xbfb8aa3b, v149
	v_exp_f32_e32 v150, v150
	v_exp_f32_e32 v151, v151
	v_add_f32_e32 v150, 1.0, v150
	v_add_f32_e32 v151, 1.0, v151
	v_rcp_f32_e32 v150, v150
	v_rcp_f32_e32 v151, v151
	v_mul_f32_e32 v148, v148, v150
	v_mul_f32_e32 v149, v149, v151
	v_mul_f32_e32 v105, v148, v71
	v_mul_f32_e32 v133, v149, v71
	v_fma_f32 v148, v176, v106, v184
	v_fma_f32 v149, v177, v134, v185
	v_fmac_f32_e32 v148, v178, v107
	v_fmac_f32_e32 v149, v179, v135
	v_fmac_f32_e32 v148, v180, v108
	v_fmac_f32_e32 v149, v181, v136
	v_fmac_f32_e32 v148, v182, v109
	v_fmac_f32_e32 v149, v183, v137
	v_mul_f32_e32 v150, 0xbfb8aa3b, v148
	v_mul_f32_e32 v151, 0xbfb8aa3b, v149
	v_exp_f32_e32 v150, v150
	v_exp_f32_e32 v151, v151
	v_add_f32_e32 v150, 1.0, v150
	v_add_f32_e32 v151, 1.0, v151
	v_rcp_f32_e32 v150, v150
	v_rcp_f32_e32 v151, v151
	v_mul_f32_e32 v148, v148, v150
	v_mul_f32_e32 v149, v149, v151
	v_mul_f32_e32 v106, v148, v72
	v_mul_f32_e32 v134, v149, v72
	v_fma_f32 v148, v176, v107, v184
	v_fma_f32 v149, v177, v135, v185
	v_fmac_f32_e32 v148, v178, v108
	v_fmac_f32_e32 v149, v179, v136
	v_fmac_f32_e32 v148, v180, v109
	v_fmac_f32_e32 v149, v181, v137
	v_fmac_f32_e32 v148, v182, v95
	v_fmac_f32_e32 v149, v183, v138
	v_mul_f32_e32 v150, 0xbfb8aa3b, v148
	v_mul_f32_e32 v151, 0xbfb8aa3b, v149
	v_exp_f32_e32 v150, v150
	v_exp_f32_e32 v151, v151
	v_add_f32_e32 v150, 1.0, v150
	v_add_f32_e32 v151, 1.0, v151
	v_rcp_f32_e32 v150, v150
	v_rcp_f32_e32 v151, v151
	v_mul_f32_e32 v148, v148, v150
	v_mul_f32_e32 v149, v149, v151
	v_mul_f32_e32 v107, v148, v73
	v_mul_f32_e32 v135, v149, v73
	s_and_b64 s[4:5], s[90:91], exec
	s_cselect_b32 s4, s51, s33
	s_add_i32 s6, 0, 0xec00
	v_cvt_pk_bf16_f32 v70, v100, v101
	v_cvt_pk_bf16_f32 v71, v102, v103
	v_cvt_pk_bf16_f32 v72, v104, v105
	v_cvt_pk_bf16_f32 v73, v106, v107
	v_cvt_pk_bf16_f32 v74, v128, v129
	v_cvt_pk_bf16_f32 v75, v130, v131
	v_cvt_pk_bf16_f32 v76, v132, v133
	v_cvt_pk_bf16_f32 v77, v134, v135
	v_add3_u32 v81, s4, v225, v226
	s_and_b64 s[4:5], s[90:91], exec
	s_cselect_b32 s4, s6, s10
	ds_write_b128 v81, v[70:73]
	ds_write_b128 v81, v[74:77] offset:272
	v_add3_u32 v70, s4, v228, v158
	ds_write_b128 v70, v[14:17]
	v_add3_u32 v70, s4, v230, v158
	ds_write_b128 v70, v[18:21]
	s_branch .LBB0_564
	s_nop 0
	s_nop 0
	s_nop 0
	s_nop 0
	s_nop 0
	s_nop 0
	s_nop 0
	s_nop 0
	s_nop 0
	s_nop 0
	s_nop 0
	s_nop 0
	s_nop 0
	s_nop 0
	s_nop 0
	s_nop 0
	s_nop 0
	s_nop 0
	s_nop 0
	s_nop 0
	s_nop 0
	s_nop 0
	s_nop 0
	s_nop 0
	s_nop 0
	s_nop 0
	s_nop 0
	s_nop 0
	s_nop 0
	s_nop 0
	s_nop 0
	s_nop 0
	s_nop 0
	s_nop 0
	s_nop 0
	s_nop 0
	s_nop 0
	s_nop 0
	s_nop 0
	s_nop 0
	s_nop 0
	s_nop 0
	s_nop 0
	s_nop 0
	s_nop 0
	s_nop 0
	s_nop 0
	s_nop 0
	s_nop 0
	s_nop 0
	s_nop 0
	s_nop 0
	s_nop 0
	s_nop 0
	s_nop 0
	s_nop 0
	s_nop 0
	s_nop 0
	s_nop 0
	s_nop 0
	s_nop 0
	s_nop 0
	s_nop 0
	s_nop 0
	s_nop 0
	s_nop 0
	s_nop 0
	s_nop 0
	s_nop 0

.LBB0_822:
	v_readlane_b32 s4, v253, 12
	s_cmp_lt_i32 s4, 9
	s_cselect_b64 s[2:3], -1, 0
	s_and_b64 s[2:3], s[2:3], s[0:1]
	s_andn2_b64 vcc, exec, s[2:3]
	v_readlane_b32 s5, v253, 13
	v_readlane_b32 s6, v253, 14
	v_readlane_b32 s7, v253, 15
	s_cbranch_vccnz .LBB0_868
	s_cmpk_gt_i32 s82, 0x3ff
	s_cbranch_scc1 .LBB0_868
	s_waitcnt vmcnt(0)
	v_lshrrev_b32_e32 v40, 4, v248
	v_readlane_b32 s4, v253, 34
	v_lshl_or_b32 v34, s84, 8, v40
	v_mov_b32_e32 v35, 0
	v_lshlrev_b32_e32 v41, 4, v248
	v_readlane_b32 s10, v253, 40
	v_readlane_b32 s11, v253, 41
	v_readlane_b32 s14, v253, 44
	v_readlane_b32 s15, v253, 45
	v_lshlrev_b64 v[36:37], 7, v[34:35]
	v_or_b32_e32 v10, 0x1c00, v41
	v_or_b32_e32 v11, 0x1800, v41
	s_mov_b64 s[10:11], s[14:15]
	v_or_b32_e32 v34, 0x1400, v41
	global_load_dwordx4 v[2:5], v10, s[10:11]
	global_load_dwordx4 v[6:9], v11, s[10:11]
	v_or_b32_e32 v38, 0x1000, v41
	global_load_dwordx4 v[10:13], v34, s[10:11]
	global_load_dwordx4 v[14:17], v38, s[10:11]
	global_load_dwordx4 v[18:21], v41, s[10:11] offset:3072
	global_load_dwordx4 v[22:25], v41, s[10:11] offset:2048
	global_load_dwordx4 v[26:29], v41, s[10:11] offset:1024
	global_load_dwordx4 v[30:33], v41, s[10:11]
	v_readlane_b32 s12, v253, 42
	v_readlane_b32 s13, v253, 43
	v_readlane_b32 s16, v253, 46
	v_readlane_b32 s17, v253, 47
	v_and_b32_e32 v1, 15, v0
	v_readlane_b32 s18, v253, 48
	v_readlane_b32 s19, v253, 49
	s_mov_b64 s[12:13], s[16:17]
	v_lshl_add_u64 v[36:37], s[12:13], 0, v[36:37]
	v_lshlrev_b32_e32 v38, 2, v1
	v_mov_b32_e32 v39, v35
	s_lshl_b32 s0, s84, 10
	v_lshl_add_u64 v[46:47], v[36:37], 0, v[38:39]
	s_add_i32 s4, s0, 0
	s_mov_b64 s[0:1], 0x2000
	v_lshl_add_u64 v[48:49], v[46:47], 0, s[0:1]
	s_mov_b64 s[0:1], 0x4000
	v_lshl_add_u64 v[50:51], v[46:47], 0, s[0:1]
	s_mov_b64 s[0:1], 0x6000
	s_lshl_b32 s34, s84, 1
	v_lshl_add_u64 v[52:53], v[46:47], 0, s[0:1]
	s_mul_i32 s0, s84, 0x3c10
	v_lshl_add_u32 v39, v40, 2, s4
	s_add_i32 s4, s4, s0
	s_or_b32 s0, s34, 1
	v_lshlrev_b32_e32 v36, 9, v40
	s_mulk_i32 s0, 0x2008
	v_and_b32_e32 v64, 31, v0
	s_mov_b64 s[14:15], s[18:19]
	v_lshl_or_b32 v40, s84, 11, v36
	s_add_i32 s0, s0, 0
	v_lshlrev_b32_e32 v36, 2, v64
	v_mov_b32_e32 v37, v35
	v_lshl_add_u64 v[54:55], s[14:15], 0, v[36:37]
	s_add_u32 s14, s92, 0x30000
	v_and_b32_e32 v37, 0x1e0, v0
	s_addc_u32 s15, s93, 0
	v_lshlrev_b32_e32 v37, 2, v37
	s_add_u32 s16, s92, 0x9e100000
	v_add3_u32 v65, 0, v37, v36
	s_addc_u32 s17, s93, 0
	v_lshlrev_b32_e32 v36, 3, v248
	v_mov_b32_e32 v37, v35
	v_lshlrev_b32_e32 v34, 2, v248
	s_add_u32 s18, s92, 0x9e300000
	v_lshl_add_u64 v[36:37], s[92:93], 0, v[36:37]
	s_mov_b64 s[10:11], 0x72100000
	v_lshrrev_b32_e32 v66, 5, v0
	s_addc_u32 s19, s93, 0
	v_lshl_add_u64 v[56:57], v[36:37], 0, s[10:11]
	v_lshl_add_u64 v[34:35], s[92:93], 0, v[34:35]
	s_mov_b64 s[10:11], 0x35c00000
	s_add_u32 s20, s92, 0x9e400000
	v_lshl_add_u64 v[58:59], v[34:35], 0, s[10:11]
	v_lshlrev_b32_e32 v34, 2, v66
	v_readlane_b32 s5, v253, 35
	s_addc_u32 s21, s93, 0
	v_lshl_or_b32 v34, s82, 6, v34
	v_readlane_b32 s6, v253, 36
	v_readlane_b32 s7, v253, 37
	v_readlane_b32 s8, v253, 38
	v_readlane_b32 s9, v253, 39
	s_movk_i32 s5, 0x2008
	v_mul_u32_u24_e32 v42, 0x2008, v1
	v_add_u32_e32 v38, 0, v38
	s_add_u32 s22, s92, 0x9e500000
	v_add_u32_e32 v60, v34, v64
	v_mbcnt_lo_u32_b32 v34, -1, 0
	s_movk_i32 s33, 0x1000
	v_mad_u32_u24 v1, v1, s5, v39
	v_add_u32_e32 v62, s4, v41
	v_add_u32_e32 v63, s0, v41
	v_cmp_gt_u32_e64 s[0:1], 4, v64
	v_cmp_eq_u32_e64 s[8:9], 0, v64
	v_cmp_eq_u32_e64 s[4:5], 1, v64
	v_cmp_eq_u32_e64 s[6:7], 2, v64
	s_addc_u32 s23, s93, 0
	s_lshl_b32 s35, s83, 6
	s_lshl_b32 s36, s82, 4
	s_lshl_b32 s37, s83, 4
	v_mov_b32_e32 v67, 0x3727c5ac
	s_mov_b32 s38, 0x800000
	v_add_u32_e32 v68, v39, v42
	v_add_u32_e32 v69, v38, v40
	v_mov_b32_e32 v70, 1
	v_mbcnt_hi_u32_b32 v71, -1, v34
	v_mov_b32_e32 v72, 0xff61b1e6
	s_mov_b32 s39, s82
	s_branch .LBB0_826
	s_nop 0
	s_nop 0
	s_nop 0
	s_nop 0
	s_nop 0
	s_nop 0
	s_nop 0
	s_nop 0

.LBB0_943:
	s_add_u32 s29, s40, 0x100
	v_mov_b32_e32 v104, 0
	s_addc_u32 s31, s41, 0
	s_mov_b32 s39, -2
	s_mov_b64 s[4:5], s[20:21]
	v_mov_b32_e32 v105, v104
	v_mov_b32_e32 v106, v104
	v_mov_b32_e32 v107, v104
	v_mov_b32_e32 v108, v104
	v_mov_b32_e32 v109, v104
	v_mov_b32_e32 v110, v104
	v_mov_b32_e32 v111, v104
	v_mov_b32_e32 v120, v104
	v_mov_b32_e32 v121, v104
	v_mov_b32_e32 v122, v104
	v_mov_b32_e32 v123, v104
	v_mov_b32_e32 v124, v104
	v_mov_b32_e32 v125, v104
	v_mov_b32_e32 v126, v104
	v_mov_b32_e32 v127, v104
	v_mov_b32_e32 v72, v104
	v_mov_b32_e32 v73, v104
	v_mov_b32_e32 v74, v104
	v_mov_b32_e32 v75, v104
	v_mov_b32_e32 v76, v104
	v_mov_b32_e32 v77, v104
	v_mov_b32_e32 v78, v104
	v_mov_b32_e32 v79, v104
	v_mov_b32_e32 v88, v104
	v_mov_b32_e32 v89, v104
	v_mov_b32_e32 v90, v104
	v_mov_b32_e32 v91, v104
	v_mov_b32_e32 v92, v104
	v_mov_b32_e32 v93, v104
	v_mov_b32_e32 v94, v104
	v_mov_b32_e32 v95, v104
	v_mov_b32_e32 v112, v104
	v_mov_b32_e32 v113, v104
	v_mov_b32_e32 v114, v104
	v_mov_b32_e32 v115, v104
	v_mov_b32_e32 v116, v104
	v_mov_b32_e32 v117, v104
	v_mov_b32_e32 v118, v104
	v_mov_b32_e32 v119, v104
	v_mov_b32_e32 v128, v104
	v_mov_b32_e32 v129, v104
	v_mov_b32_e32 v130, v104
	v_mov_b32_e32 v131, v104
	v_mov_b32_e32 v132, v104
	v_mov_b32_e32 v133, v104
	v_mov_b32_e32 v134, v104
	v_mov_b32_e32 v135, v104
	v_mov_b32_e32 v136, v104
	v_mov_b32_e32 v137, v104
	v_mov_b32_e32 v138, v104
	v_mov_b32_e32 v139, v104
	v_mov_b32_e32 v140, v104
	v_mov_b32_e32 v141, v104
	v_mov_b32_e32 v142, v104
	v_mov_b32_e32 v143, v104
	v_mov_b32_e32 v152, v104
	v_mov_b32_e32 v153, v104
	v_mov_b32_e32 v154, v104
	v_mov_b32_e32 v155, v104
	v_mov_b32_e32 v156, v104
	v_mov_b32_e32 v157, v104
	v_mov_b32_e32 v158, v104
	v_mov_b32_e32 v159, v104
	v_mov_b32_e32 v168, v104
	v_mov_b32_e32 v169, v104
	v_mov_b32_e32 v170, v104
	v_mov_b32_e32 v171, v104
	v_mov_b32_e32 v172, v104
	v_mov_b32_e32 v173, v104
	v_mov_b32_e32 v174, v104
	v_mov_b32_e32 v175, v104
	v_mov_b32_e32 v184, v104
	v_mov_b32_e32 v185, v104
	v_mov_b32_e32 v186, v104
	v_mov_b32_e32 v187, v104
	v_mov_b32_e32 v188, v104
	v_mov_b32_e32 v189, v104
	v_mov_b32_e32 v190, v104
	v_mov_b32_e32 v191, v104
	v_mov_b32_e32 v144, v104
	v_mov_b32_e32 v145, v104
	v_mov_b32_e32 v146, v104
	v_mov_b32_e32 v147, v104
	v_mov_b32_e32 v148, v104
	v_mov_b32_e32 v149, v104
	v_mov_b32_e32 v150, v104
	v_mov_b32_e32 v151, v104
	v_mov_b32_e32 v160, v104
	v_mov_b32_e32 v161, v104
	v_mov_b32_e32 v162, v104
	v_mov_b32_e32 v163, v104
	v_mov_b32_e32 v164, v104
	v_mov_b32_e32 v165, v104
	v_mov_b32_e32 v166, v104
	v_mov_b32_e32 v167, v104
	v_mov_b32_e32 v176, v104
	v_mov_b32_e32 v177, v104
	v_mov_b32_e32 v178, v104
	v_mov_b32_e32 v179, v104
	v_mov_b32_e32 v180, v104
	v_mov_b32_e32 v181, v104
	v_mov_b32_e32 v182, v104
	v_mov_b32_e32 v183, v104
	v_mov_b32_e32 v192, v104
	v_mov_b32_e32 v193, v104
	v_mov_b32_e32 v194, v104
	v_mov_b32_e32 v195, v104
	v_mov_b32_e32 v196, v104
	v_mov_b32_e32 v197, v104
	v_mov_b32_e32 v198, v104
	v_mov_b32_e32 v199, v104
	v_mov_b32_e32 v100, v104
	v_mov_b32_e32 v101, v104
	v_mov_b32_e32 v102, v104
	v_mov_b32_e32 v103, v104
	v_mov_b32_e32 v96, v104
	v_mov_b32_e32 v97, v104
	v_mov_b32_e32 v98, v104
	v_mov_b32_e32 v99, v104
	v_mov_b32_e32 v84, v104
	v_mov_b32_e32 v85, v104
	v_mov_b32_e32 v86, v104
	v_mov_b32_e32 v87, v104
	v_mov_b32_e32 v80, v104
	v_mov_b32_e32 v81, v104
	v_mov_b32_e32 v82, v104
	v_mov_b32_e32 v83, v104
	s_branch .LBB0_946
	s_nop 0
	s_nop 0
	s_nop 0
	s_nop 0
	s_nop 0
	s_nop 0
	s_nop 0
	s_nop 0
	s_nop 0
	s_nop 0
	s_nop 0
	s_nop 0
	s_nop 0
	s_nop 0
	s_nop 0
	s_nop 0
	s_nop 0
	s_nop 0
	s_nop 0
	s_nop 0
	s_nop 0
	s_nop 0
	s_nop 0
	s_nop 0
	s_nop 0
	s_nop 0
	s_nop 0
	s_nop 0
	s_nop 0
	s_nop 0
	s_nop 0
	s_nop 0
	s_nop 0
	s_nop 0
	s_nop 0
	s_nop 0
	s_nop 0
	s_nop 0
	s_nop 0
	s_nop 0
	s_nop 0
	s_nop 0
	s_nop 0
	s_nop 0
	s_nop 0
	s_nop 0
	s_nop 0
	s_nop 0
	s_nop 0
	s_nop 0
	s_nop 0
	s_nop 0
	s_nop 0
	s_nop 0
	s_nop 0
	s_nop 0
	s_nop 0
	s_nop 0
	s_nop 0
	s_nop 0
	s_nop 0

.LBB0_1029:
	s_add_u32 s31, s42, 0x100
	v_mov_b32_e32 v80, 0
	s_addc_u32 s35, s43, 0
	s_mov_b32 s41, -2
	s_mov_b64 s[4:5], s[16:17]
	v_mov_b32_e32 v81, v80
	v_mov_b32_e32 v82, v80
	v_mov_b32_e32 v83, v80
	v_mov_b32_e32 v92, v80
	v_mov_b32_e32 v93, v80
	v_mov_b32_e32 v94, v80
	v_mov_b32_e32 v95, v80
	v_mov_b32_e32 v108, v80
	v_mov_b32_e32 v109, v80
	v_mov_b32_e32 v110, v80
	v_mov_b32_e32 v111, v80
	v_mov_b32_e32 v124, v80
	v_mov_b32_e32 v125, v80
	v_mov_b32_e32 v126, v80
	v_mov_b32_e32 v127, v80
	v_mov_b32_e32 v72, v80
	v_mov_b32_e32 v73, v80
	v_mov_b32_e32 v74, v80
	v_mov_b32_e32 v75, v80
	v_mov_b32_e32 v76, v80
	v_mov_b32_e32 v77, v80
	v_mov_b32_e32 v78, v80
	v_mov_b32_e32 v79, v80
	v_mov_b32_e32 v84, v80
	v_mov_b32_e32 v85, v80
	v_mov_b32_e32 v86, v80
	v_mov_b32_e32 v87, v80
	v_mov_b32_e32 v88, v80
	v_mov_b32_e32 v89, v80
	v_mov_b32_e32 v90, v80
	v_mov_b32_e32 v91, v80
	v_mov_b32_e32 v104, v80
	v_mov_b32_e32 v105, v80
	v_mov_b32_e32 v106, v80
	v_mov_b32_e32 v107, v80
	v_mov_b32_e32 v116, v80
	v_mov_b32_e32 v117, v80
	v_mov_b32_e32 v118, v80
	v_mov_b32_e32 v119, v80
	v_mov_b32_e32 v128, v80
	v_mov_b32_e32 v129, v80
	v_mov_b32_e32 v130, v80
	v_mov_b32_e32 v131, v80
	v_mov_b32_e32 v132, v80
	v_mov_b32_e32 v133, v80
	v_mov_b32_e32 v134, v80
	v_mov_b32_e32 v135, v80
	v_mov_b32_e32 v136, v80
	v_mov_b32_e32 v137, v80
	v_mov_b32_e32 v138, v80
	v_mov_b32_e32 v139, v80
	v_mov_b32_e32 v140, v80
	v_mov_b32_e32 v141, v80
	v_mov_b32_e32 v142, v80
	v_mov_b32_e32 v143, v80
	v_mov_b32_e32 v152, v80
	v_mov_b32_e32 v153, v80
	v_mov_b32_e32 v154, v80
	v_mov_b32_e32 v155, v80
	v_mov_b32_e32 v156, v80
	v_mov_b32_e32 v157, v80
	v_mov_b32_e32 v158, v80
	v_mov_b32_e32 v159, v80
	v_mov_b32_e32 v160, v80
	v_mov_b32_e32 v161, v80
	v_mov_b32_e32 v162, v80
	v_mov_b32_e32 v163, v80
	v_mov_b32_e32 v164, v80
	v_mov_b32_e32 v165, v80
	v_mov_b32_e32 v166, v80
	v_mov_b32_e32 v167, v80
	v_mov_b32_e32 v168, v80
	v_mov_b32_e32 v169, v80
	v_mov_b32_e32 v170, v80
	v_mov_b32_e32 v171, v80
	v_mov_b32_e32 v176, v80
	v_mov_b32_e32 v177, v80
	v_mov_b32_e32 v178, v80
	v_mov_b32_e32 v179, v80
	v_mov_b32_e32 v144, v80
	v_mov_b32_e32 v145, v80
	v_mov_b32_e32 v146, v80
	v_mov_b32_e32 v147, v80
	v_mov_b32_e32 v148, v80
	v_mov_b32_e32 v149, v80
	v_mov_b32_e32 v150, v80
	v_mov_b32_e32 v151, v80
	v_mov_b32_e32 v172, v80
	v_mov_b32_e32 v173, v80
	v_mov_b32_e32 v174, v80
	v_mov_b32_e32 v175, v80
	v_mov_b32_e32 v180, v80
	v_mov_b32_e32 v181, v80
	v_mov_b32_e32 v182, v80
	v_mov_b32_e32 v183, v80
	v_mov_b32_e32 v184, v80
	v_mov_b32_e32 v185, v80
	v_mov_b32_e32 v186, v80
	v_mov_b32_e32 v187, v80
	v_mov_b32_e32 v188, v80
	v_mov_b32_e32 v189, v80
	v_mov_b32_e32 v190, v80
	v_mov_b32_e32 v191, v80
	v_mov_b32_e32 v192, v80
	v_mov_b32_e32 v193, v80
	v_mov_b32_e32 v194, v80
	v_mov_b32_e32 v195, v80
	v_mov_b32_e32 v196, v80
	v_mov_b32_e32 v197, v80
	v_mov_b32_e32 v198, v80
	v_mov_b32_e32 v199, v80
	v_mov_b32_e32 v112, v80
	v_mov_b32_e32 v113, v80
	v_mov_b32_e32 v114, v80
	v_mov_b32_e32 v115, v80
	v_mov_b32_e32 v120, v80
	v_mov_b32_e32 v121, v80
	v_mov_b32_e32 v122, v80
	v_mov_b32_e32 v123, v80
	v_mov_b32_e32 v96, v80
	v_mov_b32_e32 v97, v80
	v_mov_b32_e32 v98, v80
	v_mov_b32_e32 v99, v80
	v_mov_b32_e32 v100, v80
	v_mov_b32_e32 v101, v80
	v_mov_b32_e32 v102, v80
	v_mov_b32_e32 v103, v80
	s_branch .LBB0_1032
	s_nop 0
	s_nop 0
	s_nop 0
	s_nop 0
	s_nop 0
	s_nop 0
	s_nop 0
	s_nop 0
	s_nop 0
	s_nop 0
	s_nop 0
	s_nop 0
	s_nop 0
	s_nop 0
	s_nop 0
	s_nop 0
	s_nop 0
	s_nop 0
	s_nop 0
	s_nop 0
	s_nop 0
	s_nop 0
	s_nop 0
	s_nop 0
	s_nop 0
	s_nop 0
	s_nop 0
	s_nop 0
	s_nop 0
	s_nop 0
	s_nop 0
	s_nop 0
	s_nop 0
	s_nop 0
	s_nop 0
	s_nop 0
	s_nop 0
	s_nop 0
	s_nop 0
	s_nop 0
	s_nop 0
	s_nop 0
	s_nop 0
	s_nop 0
	s_nop 0
	s_nop 0
	s_nop 0
	s_nop 0
	s_nop 0
	s_nop 0
	s_nop 0
	s_nop 0
	s_nop 0
	s_nop 0
	s_nop 0
	s_nop 0
	s_nop 0
	s_nop 0
	s_nop 0
	s_nop 0
	s_nop 0
	s_nop 0
	s_nop 0
	s_nop 0
	s_nop 0
	s_nop 0
	s_nop 0
	s_nop 0
	s_nop 0
	s_nop 0
	s_nop 0
	s_nop 0
	s_nop 0
	s_nop 0
	s_nop 0
	s_nop 0
	s_nop 0
	s_nop 0
	s_nop 0
	s_nop 0
	s_nop 0
	s_nop 0
	s_nop 0
	s_nop 0
	s_nop 0
	s_nop 0
	s_nop 0
	s_nop 0
	s_nop 0
	s_nop 0
	s_nop 0
	s_nop 0
	s_nop 0
	s_nop 0
	s_nop 0
	s_nop 0
	s_nop 0
	s_nop 0
	s_nop 0
	s_nop 0
	s_nop 0
	s_nop 0
	s_nop 0
	s_nop 0
	s_nop 0
	s_nop 0
	s_nop 0
	s_nop 0
	s_nop 0
	s_nop 0
	s_nop 0
	s_nop 0
	s_nop 0
	s_nop 0
	s_nop 0
	s_nop 0
	s_nop 0
	s_nop 0
	s_nop 0
	s_nop 0
	s_nop 0
	s_nop 0
	s_nop 0
	s_nop 0
	s_nop 0
	s_nop 0
	s_nop 0
	s_nop 0
	s_nop 0
	s_nop 0
	s_nop 0
	s_nop 0
	s_nop 0
	s_nop 0
	s_nop 0
	s_nop 0
	s_nop 0
	s_nop 0
	s_nop 0
	s_nop 0
	s_nop 0
	s_nop 0
	s_nop 0
	s_nop 0
	s_nop 0
	s_nop 0
	s_nop 0
	s_nop 0
	s_nop 0
	s_nop 0
	s_nop 0
	s_nop 0
	s_nop 0
	s_nop 0
	s_nop 0
	s_nop 0
	s_nop 0
	s_nop 0
	s_nop 0
	s_nop 0
	s_nop 0
	s_nop 0
	s_nop 0
	s_nop 0
	s_nop 0
	s_nop 0
	s_nop 0
	s_nop 0
	s_nop 0
	s_nop 0
	s_nop 0
	s_nop 0
	s_nop 0
	s_nop 0
	s_nop 0
	s_nop 0
	s_nop 0
	s_nop 0
	s_nop 0
	s_nop 0
	s_nop 0
	s_nop 0
	s_nop 0
	s_nop 0
	s_nop 0
	s_nop 0
	s_nop 0
	s_nop 0
	s_nop 0
	s_nop 0
	s_nop 0
	s_nop 0
	s_nop 0
	s_nop 0
	s_nop 0
	s_nop 0
	s_nop 0
	s_nop 0
	s_nop 0
	s_nop 0
	s_nop 0
	s_nop 0
	s_nop 0
	s_nop 0
	s_nop 0
	s_nop 0
	s_nop 0
	s_nop 0
	s_nop 0
	s_nop 0
	s_nop 0
	s_nop 0
	s_nop 0
	s_nop 0
	s_nop 0
	s_nop 0
	s_nop 0
	s_nop 0
	s_nop 0
	s_nop 0
	s_nop 0
	s_nop 0
	s_nop 0
	s_nop 0
	s_nop 0
	s_nop 0
	s_nop 0
	s_nop 0
	s_nop 0
	s_nop 0
